# layer2 W2-dot on MFMA interleaved into last k-step (batch-tile-major), 8 partials/row, 2-read reduce, permlane hand-off, noise prefetch
# speedup vs baseline: 1.0184x; 1.0184x over previous
.LBB1_2:
	v_lshrrev_b32_e32 v151, 4, v137
	s_lshl_b64 s[6:7], s[2:3], 4
	v_cmp_eq_u32_e64 s[2:3], 1, v151
	s_waitcnt vmcnt(31)
	v_cvt_f16_f32_e32 v8, v8
	v_cmp_gt_u32_e32 vcc, 16, v137
	s_waitcnt vmcnt(29)
	v_cndmask_b32_e64 v116, 0, v116, s[2:3]
	s_waitcnt vmcnt(21)
	v_cndmask_b32_e64 v100, 0, v100, s[2:3]
	v_cmp_eq_u32_e64 s[0:1], 2, v151
	v_cndmask_b32_e64 v114, 0, v114, s[2:3]
	v_cndmask_b32_e64 v115, 0, v115, s[2:3]
	v_cndmask_b32_e32 v6, v116, v6, vcc
	v_cndmask_b32_e64 v116, 0, v117, s[2:3]
	v_cndmask_b32_e64 v108, 0, v108, s[2:3]
	v_cndmask_b32_e32 v26, v100, v26, vcc
	v_cvt_f16_f32_e32 v29, v29
	v_cndmask_b32_e64 v100, 0, v101, s[2:3]
	v_cndmask_b32_e32 v28, 0, v28, vcc
	v_cndmask_b32_e64 v152, 0, 1.0, s[0:1]
	v_cndmask_b32_e32 v114, v114, v120, vcc
	v_cndmask_b32_e32 v115, v115, v121, vcc
	v_cndmask_b32_e32 v7, v116, v7, vcc
	v_cndmask_b32_e64 v106, 0, v106, s[2:3]
	v_cndmask_b32_e64 v107, 0, v107, s[2:3]
	v_cndmask_b32_e32 v14, v108, v14, vcc
	v_cndmask_b32_e64 v108, 0, v109, s[2:3]
	v_cndmask_b32_e32 v27, v100, v27, vcc
	v_cvt_f16_f32_e32 v100, v28
	v_cndmask_b32_e32 v116, 0, v8, vcc
	v_cvt_pk_f16_f32 v8, v6, v7
	v_cvt_pk_f16_f32 v7, v114, v115
	v_cndmask_b32_e64 v114, v152, v140, s[2:3]
	v_cndmask_b32_e32 v106, v106, v112, vcc
	v_cndmask_b32_e32 v107, v107, v113, vcc
	v_cndmask_b32_e32 v15, v108, v15, vcc
	v_cndmask_b32_e64 v98, 0, v98, s[2:3]
	v_cndmask_b32_e64 v99, 0, v99, s[2:3]
	v_cndmask_b32_e32 v110, v114, v110, vcc
	v_cndmask_b32_e64 v114, 0, v141, s[2:3]
	v_cndmask_b32_e32 v108, 0, v16, vcc
	v_cvt_pk_f16_f32 v16, v14, v15
	v_cvt_pk_f16_f32 v15, v106, v107
	v_cndmask_b32_e64 v106, v152, v138, s[2:3]
	v_cndmask_b32_e32 v98, v98, v104, vcc
	v_cndmask_b32_e32 v99, v99, v105, vcc
	v_cndmask_b32_e32 v111, v114, v111, vcc
	v_cndmask_b32_e32 v102, v106, v102, vcc
	v_cndmask_b32_e64 v106, 0, v139, s[2:3]
	v_cndmask_b32_e32 v29, 0, v29, vcc
	v_cvt_pk_f16_f32 v28, v26, v27
	v_cvt_pk_f16_f32 v27, v98, v99
	v_lshlrev_b32_e32 v101, 10, v1
	v_bitop3_b32 v98, v151, v0, 3 bitop3:0x78
	v_lshl_add_u64 v[130:131], s[4:5], 0, v[130:131]
	v_cvt_f16_f32_e32 v4, v4
	v_cvt_pk_f16_f32 v14, v110, v111
	v_cndmask_b32_e32 v103, v106, v103, vcc
	v_pack_b32_f16 v29, v100, v29
	v_lshl_or_b32 v111, v98, 4, v101
	v_lshlrev_b32_e32 v100, 4, v1
	s_movk_i32 s4, 0xc0
	v_cndmask_b32_e64 v124, 0, v124, s[2:3]
	v_cvt_pk_f16_f32 v26, v102, v103
	v_and_b32_e32 v112, 0xc0, v100
	v_bitop3_b32 v100, v100, s4, v111 bitop3:0x26
	s_lshl_b32 s4, s20, 3
	v_lshrrev_b32_e32 v102, 5, v137
	v_lshrrev_b32_e32 v104, 1, v137
	v_cndmask_b32_e64 v122, 0, v122, s[2:3]
	v_cndmask_b32_e64 v123, 0, v123, s[2:3]
	v_cndmask_b32_e32 v2, v124, v2, vcc
	v_cvt_f16_f32_e32 v5, v5
	v_cndmask_b32_e64 v124, 0, v125, s[2:3]
	v_cvt_f16_f32_e32 v9, v9
	v_or_b32_e32 v103, s4, v102
	v_and_or_b32 v110, v104, 8, v101
	v_bitop3_b32 v101, s4, v1, v102 bitop3:0x36
	s_lshl_b32 s4, s20, 4
	v_cndmask_b32_e32 v122, v122, v128, vcc
	v_cndmask_b32_e32 v123, v123, v129, vcc
	v_cndmask_b32_e32 v3, v124, v3, vcc
	v_cndmask_b32_e32 v17, 0, v17, vcc
	v_lshlrev_b32_e32 v107, 4, v101
	v_bitop3_b32 v101, v103, v1, 2 bitop3:0x36
	s_add_i32 s4, s4, 0x10000
	v_bfe_u32 v0, v0, 4, 2
	v_cndmask_b32_e64 v144, v152, v144, s[2:3]
	v_cndmask_b32_e32 v124, 0, v4, vcc
	v_cvt_pk_f16_f32 v4, v2, v3
	v_cvt_pk_f16_f32 v3, v122, v123
	v_cndmask_b32_e64 v122, v152, v142, s[2:3]
	v_cvt_pk_f16_f32 v17, v108, v17
	s_movk_i32 s5, 0x80
	v_lshlrev_b32_e32 v108, 4, v101
	v_bitop3_b32 v101, v103, v1, 4 bitop3:0x36
	s_cmp_lt_u32 s22, 64
	v_lshlrev_b32_e32 v104, 5, v0
	v_lshlrev_b32_e32 v0, 6, v0
	v_cndmask_b32_e32 v126, v144, v126, vcc
	v_cndmask_b32_e64 v144, 0, v145, s[2:3]
	v_cndmask_b32_e32 v118, v122, v118, vcc
	v_cndmask_b32_e64 v122, 0, v143, s[2:3]
	v_bitop3_b32 v99, v112, s5, v111 bitop3:0x36
	v_lshlrev_b32_e32 v109, 4, v101
	v_bitop3_b32 v101, v103, v1, 6 bitop3:0x36
	v_lshl_or_b32 v105, s20, 8, v0
	v_mov_b32_e32 v0, 0x1ec00
	s_cselect_b64 s[4:5], -1, 0
	v_cndmask_b32_e32 v127, v144, v127, vcc
	v_cndmask_b32_e32 v5, 0, v5, vcc
	v_cndmask_b32_e32 v119, v122, v119, vcc
	v_cndmask_b32_e32 v9, 0, v9, vcc
	v_lshlrev_b32_e32 v113, 4, v101
	v_lshlrev_b32_e32 v101, 5, v1
	v_lshl_add_u32 v106, v137, 6, v0
	v_cndmask_b32_e64 v0, 0, 1, s[4:5]
	v_lshl_add_u64 v[132:133], s[8:9], 0, v[132:133]
	v_or_b32_e32 v148, 0x400, v147
	v_or_b32_e32 v149, 0x800, v147
	v_or_b32_e32 v150, 0xc00, v147
	v_cvt_pk_f16_f32 v2, v126, v127
	v_pack_b32_f16 v5, v124, v5
	v_cvt_pk_f16_f32 v6, v118, v119
	v_pack_b32_f16 v9, v116, v9
	v_bitop3_b32 v98, v112, 64, v111 bitop3:0x36
	v_lshl_or_b32 v104, s20, 7, v104
	s_mov_b32 s22, 0x98000
	s_mov_b32 s23, 0x5040100
	s_mov_b32 s24, 0x7060302
	v_add_u32_e32 v107, v107, v110
	v_add_u32_e32 v108, v108, v110
	v_add_u32_e32 v109, v109, v110
	v_add_u32_e32 v110, v113, v110
	v_add_u32_e32 v111, v112, v111
	v_lshlrev_b32_e32 v113, 4, v137
	v_or_b32_e32 v113, 0x10000, v113
	s_lshr_b32 s28, s20, 2
	s_and_b32 s29, s20, 3
	s_lshl_b32 s28, s28, 10
	s_lshl_b32 s29, s29, 2
	s_add_i32 s28, s28, s29
	v_add_u32_e32 v112, s28, v113
	v_cmp_eq_u32_e64 s[26:27], 3, v151
	v_add_u32_e32 v114, 0x12400, v101
	v_cmp_ne_u32_e64 s[4:5], 1, v0
	v_mov_b32_e32 v121, v136
	v_mov_b32_e32 v144, v136
	v_mov_b32_e32 v0, v136
	v_mov_b32_e32 v1, v136
	s_waitcnt lgkmcnt(0)
	s_barrier
	ds_read_u16 v248, v114
	ds_read_u16 v249, v114 offset:512
	ds_read_u16 v250, v114 offset:1024
	ds_read_u16 v251, v114 offset:1536
	v_add_u32_e32 v114, 2, v114
	s_branch .LBB1_4
.LBB1_3:
	s_add_i32 s22, s22, 0x80000
	s_add_i32 s11, s11, 1
	s_add_u32 s12, s12, 4
	s_addc_u32 s13, s13, 0
	v_add_u32_e32 v104, 0x400, v104
	v_add_u32_e32 v105, 0x800, v105
	v_add_u32_e32 v106, 4, v106
	s_cmp_eq_u32 s22, 0x898000
	v_add_u32_e32 v114, 2, v114
	s_cbranch_scc1 .LBB1_8
.LBB1_4:
	s_waitcnt lgkmcnt(0)
	s_and_saveexec_b64 s[8:9], s[2:3]
	v_cvt_f16_f32_e32 v0, v0
	v_cvt_f16_f32_e32 v1, v1
	v_cvt_f16_f32_e32 v121, v121
	v_cvt_f16_f32_e32 v144, v144
	v_perm_b32 v5, v0, v248, s23
	v_perm_b32 v9, v1, v249, s23
	v_perm_b32 v17, v121, v250, s23
	v_perm_b32 v29, v144, v251, s23
	s_or_b64 exec, exec, s[8:9]
	s_waitcnt vmcnt(16)
	v_cndmask_b32_e64 v0, v30, v134, s[0:1]
	v_bfi_b32 v30, s10, v0, v30
	v_perm_b32 v0, v22, v134, s24
	v_cndmask_b32_e64 v22, v22, v0, s[0:1]
	v_bfi_b32 v1, s10, v135, v18
	v_perm_b32 v0, v10, v135, s24
	v_mfma_f32_16x16x32_f16 v[126:129], v[30:33], v[6:9], 0
	v_cndmask_b32_e64 v18, v18, v1, s[0:1]
	v_cndmask_b32_e64 v10, v10, v0, s[0:1]
	s_cmp_lg_u32 s22, 0x818000
	v_mfma_f32_16x16x32_f16 v[122:125], v[30:33], v[2:5], 0
	s_cselect_b32 s9, s11, 15
	s_nop 2
	v_cvt_pk_f16_f32 v121, v126, v127
	v_cvt_pk_f16_f32 v127, v128, v129
	v_mfma_f32_16x16x32_f16 v[134:137], v[30:33], v[14:17], 0
	v_pk_max_f16 v126, v121, 0
	s_nop 0
	v_cvt_pk_f16_f32 v0, v122, v123
	v_cvt_pk_f16_f32 v1, v124, v125
	v_mfma_f32_16x16x32_f16 v[30:33], v[30:33], v[26:29], 0
	v_pk_max_f16 v127, v127, 0
	v_pk_max_f16 v0, v0, 0
	v_pk_max_f16 v1, v1, 0
	v_mfma_f32_16x16x32_f16 v[122:125], v[22:25], v[2:5], 0
	ds_write2st64_b64 v107, v[0:1], v[126:127] offset1:32
	s_nop 1
	v_cvt_pk_f16_f32 v0, v134, v135
	v_cvt_pk_f16_f32 v1, v136, v137
	v_mfma_f32_16x16x32_f16 v[126:129], v[22:25], v[6:9], 0
	s_nop 0
	v_cvt_pk_f16_f32 v30, v30, v31
	v_cvt_pk_f16_f32 v31, v32, v33
	v_pk_max_f16 v0, v0, 0
	v_mfma_f32_16x16x32_f16 v[134:137], v[22:25], v[14:17], 0
	v_pk_max_f16 v30, v30, 0
	v_pk_max_f16 v31, v31, 0
	v_pk_max_f16 v1, v1, 0
	v_mfma_f32_16x16x32_f16 v[22:25], v[22:25], v[26:29], 0
	ds_write2st64_b64 v107, v[0:1], v[30:31] offset0:64 offset1:96
	v_cvt_pk_f16_f32 v0, v122, v123
	v_cvt_pk_f16_f32 v1, v124, v125
	v_mfma_f32_16x16x32_f16 v[30:33], v[18:21], v[2:5], 0
	v_pk_max_f16 v0, v0, 0
	v_cvt_pk_f16_f32 v139, v128, v129
	v_pk_max_f16 v1, v1, 0
	v_mfma_f32_16x16x32_f16 v[122:125], v[18:21], v[6:9], 0
	v_cvt_pk_f16_f32 v121, v126, v127
	v_pk_max_f16 v138, v121, 0
	v_pk_max_f16 v139, v139, 0
	v_mfma_f32_16x16x32_f16 v[126:129], v[18:21], v[14:17], 0
	ds_write2st64_b64 v108, v[0:1], v[138:139] offset1:32
	v_cvt_pk_f16_f32 v0, v134, v135
	v_cvt_pk_f16_f32 v1, v136, v137
	v_mfma_f32_16x16x32_f16 v[18:21], v[18:21], v[26:29], 0
	v_pk_max_f16 v0, v0, 0
	v_cvt_pk_f16_f32 v139, v24, v25
	v_pk_max_f16 v1, v1, 0
	v_mfma_f32_16x16x32_f16 v[134:137], v[10:13], v[2:5], 0
	v_cvt_pk_f16_f32 v121, v22, v23
	v_pk_max_f16 v138, v121, 0
	v_pk_max_f16 v139, v139, 0
	ds_write2st64_b64 v108, v[0:1], v[138:139] offset0:64 offset1:96
	v_cvt_pk_f16_f32 v0, v30, v31
	v_mfma_f32_16x16x32_f16 v[22:25], v[10:13], v[6:9], 0
	v_cvt_pk_f16_f32 v1, v32, v33
	v_pk_max_f16 v0, v0, 0
	v_cvt_pk_f16_f32 v30, v122, v123
	v_cvt_pk_f16_f32 v31, v124, v125
	v_mfma_f32_16x16x32_f16 v[138:141], v[10:13], v[14:17], 0
	v_pk_max_f16 v1, v1, 0
	v_pk_max_f16 v30, v30, 0
	v_pk_max_f16 v31, v31, 0
	ds_write2st64_b64 v109, v[0:1], v[30:31] offset1:32
	v_cvt_pk_f16_f32 v0, v126, v127
	v_mfma_f32_16x16x32_f16 v[10:13], v[10:13], v[26:29], 0
	v_cvt_pk_f16_f32 v1, v128, v129
	v_pk_max_f16 v0, v0, 0
	v_cvt_pk_f16_f32 v18, v18, v19
	v_cvt_pk_f16_f32 v19, v20, v21
	v_pk_max_f16 v1, v1, 0
	v_pk_max_f16 v18, v18, 0
	v_pk_max_f16 v19, v19, 0
	ds_write2st64_b64 v109, v[0:1], v[18:19] offset0:64 offset1:96
	v_cvt_pk_f16_f32 v0, v134, v135
	v_cvt_pk_f16_f32 v1, v136, v137
	v_pk_max_f16 v0, v0, 0
	v_cvt_pk_f16_f32 v18, v22, v23
	v_cvt_pk_f16_f32 v19, v24, v25
	v_pk_max_f16 v1, v1, 0
	v_pk_max_f16 v18, v18, 0
	v_pk_max_f16 v19, v19, 0
	ds_write2st64_b64 v110, v[0:1], v[18:19] offset1:32
	v_cvt_pk_f16_f32 v0, v138, v139
	v_cvt_pk_f16_f32 v1, v140, v141
	v_pk_max_f16 v0, v0, 0
	v_cvt_pk_f16_f32 v10, v10, v11
	v_cvt_pk_f16_f32 v11, v12, v13
	v_pk_max_f16 v1, v1, 0
	v_pk_max_f16 v10, v10, 0
	v_pk_max_f16 v11, v11, 0
	ds_write2st64_b64 v110, v[0:1], v[10:11] offset0:64 offset1:96
	v_add_u32_e32 v0, 0x12c00, v105
	s_waitcnt lgkmcnt(0)
	s_barrier
	v_add_u32_e32 v1, 0x12c10, v105
	ds_read_b128 v[10:13], v0
	ds_read_b128 v[18:21], v1
	v_add_u32_e32 v0, 0x12c20, v105
	v_add_u32_e32 v1, 0x12c30, v105
	ds_read_b128 v[22:25], v0
	ds_read_b128 v[30:33], v1
	ds_read_b128 v[122:125], v111
	ds_read_b128 v[126:129], v111 offset:16384
	ds_read_b128 v[134:137], v111 offset:32768
	ds_read_b128 v[138:141], v111 offset:49152
	ds_read_b128 v[142:145], v98
	ds_read_b128 v[152:155], v98 offset:16384
	ds_read_b128 v[156:159], v98 offset:32768
	ds_read_b128 v[160:163], v98 offset:49152
	s_lshl_b32 s20, s9, 7
	v_lshl_add_u64 v[0:1], s[20:21], 3, v[132:133]
	s_add_i32 s25, s22, 0xfff88000
	s_lshl_b32 s8, s9, 8
	buffer_load_dwordx4 v[192:195], v147, s[16:19], s25 offen
	buffer_load_dwordx4 v[196:199], v148, s[16:19], s25 offen
	buffer_load_dwordx4 v[200:203], v149, s[16:19], s25 offen
	buffer_load_dwordx4 v[204:207], v150, s[16:19], s25 offen
	s_waitcnt vmcnt(19) lgkmcnt(7)
	v_mfma_f32_16x16x32_f16 v[164:167], v[58:61], v[122:125], v[10:13]
	s_waitcnt lgkmcnt(6)
	v_mfma_f32_16x16x32_f16 v[168:171], v[58:61], v[126:129], v[10:13]
	s_waitcnt lgkmcnt(5)
	v_mfma_f32_16x16x32_f16 v[172:175], v[58:61], v[134:137], v[10:13]
	s_waitcnt lgkmcnt(4)
	v_mfma_f32_16x16x32_f16 v[10:13], v[58:61], v[138:141], v[10:13]
	s_waitcnt vmcnt(18)
	v_mfma_f32_16x16x32_f16 v[58:61], v[54:57], v[122:125], v[18:21]
	v_mfma_f32_16x16x32_f16 v[176:179], v[54:57], v[126:129], v[18:21]
	v_mfma_f32_16x16x32_f16 v[180:183], v[54:57], v[134:137], v[18:21]
	v_mfma_f32_16x16x32_f16 v[18:21], v[54:57], v[138:141], v[18:21]
	s_waitcnt vmcnt(17)
	v_mfma_f32_16x16x32_f16 v[54:57], v[50:53], v[122:125], v[22:25]
	v_mfma_f32_16x16x32_f16 v[184:187], v[50:53], v[126:129], v[22:25]
	v_mfma_f32_16x16x32_f16 v[188:191], v[50:53], v[134:137], v[22:25]
	v_mfma_f32_16x16x32_f16 v[22:25], v[50:53], v[138:141], v[22:25]
	s_waitcnt vmcnt(16)
	v_mfma_f32_16x16x32_f16 v[50:53], v[38:41], v[122:125], v[30:33]
	v_mfma_f32_16x16x32_f16 v[122:125], v[38:41], v[126:129], v[30:33]
	v_mfma_f32_16x16x32_f16 v[126:129], v[38:41], v[134:137], v[30:33]
	v_mfma_f32_16x16x32_f16 v[38:41], v[38:41], v[138:141], v[30:33]
	ds_read_b128 v[136:139], v99
	ds_read_b128 v[208:211], v99 offset:16384
	ds_read_b128 v[212:215], v99 offset:32768
	ds_read_b128 v[216:219], v99 offset:49152
	s_add_i32 s9, s22, 0xfff90000
	s_waitcnt vmcnt(15) lgkmcnt(7)
	v_mfma_f32_16x16x32_f16 v[164:167], v[94:97], v[142:145], v[164:167]
	s_waitcnt lgkmcnt(6)
	v_mfma_f32_16x16x32_f16 v[168:171], v[94:97], v[152:155], v[168:171]
	s_waitcnt vmcnt(14)
	v_mfma_f32_16x16x32_f16 v[58:61], v[90:93], v[142:145], v[58:61]
	v_mfma_f32_16x16x32_f16 v[176:179], v[90:93], v[152:155], v[176:179]
	s_waitcnt vmcnt(13)
	v_mfma_f32_16x16x32_f16 v[54:57], v[78:81], v[142:145], v[54:57]
	v_mfma_f32_16x16x32_f16 v[184:187], v[78:81], v[152:155], v[184:187]
	s_waitcnt vmcnt(12)
	v_mfma_f32_16x16x32_f16 v[50:53], v[34:37], v[142:145], v[50:53]
	buffer_load_dwordx4 v[140:143], v147, s[16:19], s9 offen
	buffer_load_dwordx4 v[220:223], v148, s[16:19], s9 offen
	v_mfma_f32_16x16x32_f16 v[122:125], v[34:37], v[152:155], v[122:125]
	buffer_load_dwordx4 v[152:155], v149, s[16:19], s9 offen
	buffer_load_dwordx4 v[224:227], v150, s[16:19], s9 offen
	s_mov_b32 s9, s21
	s_waitcnt lgkmcnt(5)
	v_mfma_f32_16x16x32_f16 v[172:175], v[94:97], v[156:159], v[172:175]
	s_waitcnt lgkmcnt(4)
	v_mfma_f32_16x16x32_f16 v[94:97], v[94:97], v[160:163], v[10:13]
	s_nop 2
	v_lshl_add_u64 v[10:11], s[8:9], 4, v[130:131]
	v_mfma_f32_16x16x32_f16 v[180:183], v[90:93], v[156:159], v[180:183]
	v_mfma_f32_16x16x32_f16 v[90:93], v[90:93], v[160:163], v[18:21]
	v_mfma_f32_16x16x32_f16 v[188:191], v[78:81], v[156:159], v[188:191]
	v_mfma_f32_16x16x32_f16 v[78:81], v[78:81], v[160:163], v[22:25]
	global_load_dwordx4 v[30:33], v[10:11], off
	s_nop 1
	global_load_dwordx4 v[22:25], v[10:11], off offset:1024
	global_load_dwordx4 v[18:21], v[10:11], off offset:2048
	s_nop 0
	global_load_dwordx4 v[10:13], v[10:11], off offset:3072
	s_nop 0
	global_load_dwordx2 v[134:135], v[0:1], off
	v_mfma_f32_16x16x32_f16 v[126:129], v[34:37], v[156:159], v[126:129]
	v_mfma_f32_16x16x32_f16 v[34:37], v[34:37], v[160:163], v[38:41]
	s_nop 2
	ds_read_b128 v[38:41], v100
	ds_read_b128 v[156:159], v100 offset:16384
	ds_read_b128 v[160:163], v100 offset:32768
	ds_read_b128 v[228:231], v100 offset:49152
	s_add_i32 s8, s22, 0xfff98000
	s_waitcnt vmcnt(20) lgkmcnt(7)
	v_mfma_f32_16x16x32_f16 v[164:167], v[82:85], v[136:139], v[164:167]
	s_waitcnt lgkmcnt(6)
	v_mfma_f32_16x16x32_f16 v[168:171], v[82:85], v[208:211], v[168:171]
	s_waitcnt lgkmcnt(5)
	v_mfma_f32_16x16x32_f16 v[172:175], v[82:85], v[212:215], v[172:175]
	s_waitcnt lgkmcnt(4)
	v_mfma_f32_16x16x32_f16 v[82:85], v[82:85], v[216:219], v[94:97]
	s_waitcnt vmcnt(19)
	v_mfma_f32_16x16x32_f16 v[58:61], v[70:73], v[136:139], v[58:61]
	v_mfma_f32_16x16x32_f16 v[94:97], v[70:73], v[208:211], v[176:179]
	v_mfma_f32_16x16x32_f16 v[176:179], v[70:73], v[212:215], v[180:183]
	v_mfma_f32_16x16x32_f16 v[70:73], v[70:73], v[216:219], v[90:93]
	s_waitcnt vmcnt(18)
	v_mfma_f32_16x16x32_f16 v[54:57], v[62:65], v[136:139], v[54:57]
	v_mfma_f32_16x16x32_f16 v[90:93], v[62:65], v[208:211], v[184:187]
	v_mfma_f32_16x16x32_f16 v[180:183], v[62:65], v[212:215], v[188:191]
	v_mfma_f32_16x16x32_f16 v[62:65], v[62:65], v[216:219], v[78:81]
	s_waitcnt vmcnt(17)
	v_mfma_f32_16x16x32_f16 v[50:53], v[42:45], v[136:139], v[50:53]
	v_mfma_f32_16x16x32_f16 v[78:81], v[42:45], v[208:211], v[122:125]
	v_mfma_f32_16x16x32_f16 v[122:125], v[42:45], v[212:215], v[126:129]
	s_nop 2
	buffer_load_dwordx4 v[126:129], v147, s[16:19], s8 offen
	buffer_load_dwordx4 v[136:139], v148, s[16:19], s8 offen
	buffer_load_dwordx4 v[184:187], v149, s[16:19], s8 offen
	buffer_load_dwordx4 v[188:191], v150, s[16:19], s8 offen
	v_mfma_f32_16x16x32_f16 v[34:37], v[42:45], v[216:219], v[34:37]
	ds_read_b128 v[42:45], v111 offset:256
	ds_read_b128 v[208:211], v111 offset:16640
	ds_read_b128 v[212:215], v111 offset:33024
	ds_read_b128 v[216:219], v111 offset:49408
	s_add_i32 s8, s22, 0xfffa0000
	s_waitcnt vmcnt(20) lgkmcnt(7)
	v_mfma_f32_16x16x32_f16 v[164:167], v[86:89], v[38:41], v[164:167]
	s_waitcnt lgkmcnt(6)
	v_mfma_f32_16x16x32_f16 v[168:171], v[86:89], v[156:159], v[168:171]
	s_waitcnt lgkmcnt(5)
	v_mfma_f32_16x16x32_f16 v[172:175], v[86:89], v[160:163], v[172:175]
	s_waitcnt lgkmcnt(4)
	v_mfma_f32_16x16x32_f16 v[82:85], v[86:89], v[228:231], v[82:85]
	s_waitcnt vmcnt(19)
	v_mfma_f32_16x16x32_f16 v[58:61], v[74:77], v[38:41], v[58:61]
	v_mfma_f32_16x16x32_f16 v[86:89], v[74:77], v[156:159], v[94:97]
	v_mfma_f32_16x16x32_f16 v[94:97], v[74:77], v[160:163], v[176:179]
	v_mfma_f32_16x16x32_f16 v[70:73], v[74:77], v[228:231], v[70:73]
	s_waitcnt vmcnt(18)
	v_mfma_f32_16x16x32_f16 v[54:57], v[66:69], v[38:41], v[54:57]
	v_mfma_f32_16x16x32_f16 v[74:77], v[66:69], v[156:159], v[90:93]
	v_mfma_f32_16x16x32_f16 v[90:93], v[66:69], v[160:163], v[180:183]
	v_mfma_f32_16x16x32_f16 v[62:65], v[66:69], v[228:231], v[62:65]
	s_waitcnt vmcnt(17)
	v_mfma_f32_16x16x32_f16 v[38:41], v[46:49], v[38:41], v[50:53]
	v_mfma_f32_16x16x32_f16 v[50:53], v[46:49], v[156:159], v[78:81]
	v_mfma_f32_16x16x32_f16 v[66:69], v[46:49], v[160:163], v[122:125]
	s_nop 1
	buffer_load_dwordx4 v[78:81], v147, s[16:19], s8 offen
	buffer_load_dwordx4 v[122:125], v148, s[16:19], s8 offen
	buffer_load_dwordx4 v[156:159], v149, s[16:19], s8 offen
	buffer_load_dwordx4 v[160:163], v150, s[16:19], s8 offen
	v_mfma_f32_16x16x32_f16 v[34:37], v[46:49], v[228:231], v[34:37]
	ds_read_b128 v[46:49], v98 offset:256
	ds_read_b128 v[176:179], v98 offset:16640
	ds_read_b128 v[180:183], v98 offset:33024
	ds_read_b128 v[228:231], v98 offset:49408
	s_add_i32 s8, s22, 0xfffa8000
	s_waitcnt vmcnt(20) lgkmcnt(7)
	v_mfma_f32_16x16x32_f16 v[164:167], v[192:195], v[42:45], v[164:167]
	s_waitcnt lgkmcnt(6)
	v_mfma_f32_16x16x32_f16 v[168:171], v[192:195], v[208:211], v[168:171]
	s_waitcnt lgkmcnt(5)
	v_mfma_f32_16x16x32_f16 v[172:175], v[192:195], v[212:215], v[172:175]
	s_waitcnt lgkmcnt(4)
	v_mfma_f32_16x16x32_f16 v[82:85], v[192:195], v[216:219], v[82:85]
	s_waitcnt vmcnt(19)
	v_mfma_f32_16x16x32_f16 v[58:61], v[196:199], v[42:45], v[58:61]
	v_mfma_f32_16x16x32_f16 v[86:89], v[196:199], v[208:211], v[86:89]
	v_mfma_f32_16x16x32_f16 v[94:97], v[196:199], v[212:215], v[94:97]
	v_mfma_f32_16x16x32_f16 v[70:73], v[196:199], v[216:219], v[70:73]
	s_waitcnt vmcnt(18)
	v_mfma_f32_16x16x32_f16 v[54:57], v[200:203], v[42:45], v[54:57]
	v_mfma_f32_16x16x32_f16 v[74:77], v[200:203], v[208:211], v[74:77]
	v_mfma_f32_16x16x32_f16 v[90:93], v[200:203], v[212:215], v[90:93]
	v_mfma_f32_16x16x32_f16 v[62:65], v[200:203], v[216:219], v[62:65]
	s_waitcnt vmcnt(17)
	v_mfma_f32_16x16x32_f16 v[38:41], v[204:207], v[42:45], v[38:41]
	v_mfma_f32_16x16x32_f16 v[42:45], v[204:207], v[208:211], v[50:53]
	v_mfma_f32_16x16x32_f16 v[50:53], v[204:207], v[212:215], v[66:69]
	s_nop 2
	buffer_load_dwordx4 v[66:69], v147, s[16:19], s8 offen
	buffer_load_dwordx4 v[192:195], v148, s[16:19], s8 offen
	buffer_load_dwordx4 v[196:199], v149, s[16:19], s8 offen
	buffer_load_dwordx4 v[200:203], v150, s[16:19], s8 offen
	v_mfma_f32_16x16x32_f16 v[34:37], v[204:207], v[216:219], v[34:37]
	ds_read_b128 v[204:207], v99 offset:256
	ds_read_b128 v[208:211], v99 offset:16640
	ds_read_b128 v[212:215], v99 offset:33024
	ds_read_b128 v[216:219], v99 offset:49408
	s_add_i32 s8, s22, 0xfffb0000
	s_waitcnt vmcnt(20) lgkmcnt(7)
	v_mfma_f32_16x16x32_f16 v[164:167], v[140:143], v[46:49], v[164:167]
	s_waitcnt lgkmcnt(6)
	v_mfma_f32_16x16x32_f16 v[168:171], v[140:143], v[176:179], v[168:171]
	s_waitcnt lgkmcnt(5)
	v_mfma_f32_16x16x32_f16 v[172:175], v[140:143], v[180:183], v[172:175]
	s_waitcnt lgkmcnt(4)
	v_mfma_f32_16x16x32_f16 v[82:85], v[140:143], v[228:231], v[82:85]
	s_waitcnt vmcnt(19)
	v_mfma_f32_16x16x32_f16 v[58:61], v[220:223], v[46:49], v[58:61]
	v_mfma_f32_16x16x32_f16 v[86:89], v[220:223], v[176:179], v[86:89]
	s_waitcnt vmcnt(18)
	v_mfma_f32_16x16x32_f16 v[54:57], v[152:155], v[46:49], v[54:57]
	v_mfma_f32_16x16x32_f16 v[74:77], v[152:155], v[176:179], v[74:77]
	v_mfma_f32_16x16x32_f16 v[90:93], v[152:155], v[180:183], v[90:93]
	v_mfma_f32_16x16x32_f16 v[62:65], v[152:155], v[228:231], v[62:65]
	s_waitcnt vmcnt(17)
	v_mfma_f32_16x16x32_f16 v[38:41], v[224:227], v[46:49], v[38:41]
	v_mfma_f32_16x16x32_f16 v[42:45], v[224:227], v[176:179], v[42:45]
	v_mfma_f32_16x16x32_f16 v[46:49], v[224:227], v[180:183], v[50:53]
	s_nop 2
	buffer_load_dwordx4 v[50:53], v147, s[16:19], s8 offen
	buffer_load_dwordx4 v[140:143], v148, s[16:19], s8 offen
	buffer_load_dwordx4 v[152:155], v149, s[16:19], s8 offen
	buffer_load_dwordx4 v[176:179], v150, s[16:19], s8 offen
	v_mfma_f32_16x16x32_f16 v[94:97], v[220:223], v[180:183], v[94:97]
	v_mfma_f32_16x16x32_f16 v[70:73], v[220:223], v[228:231], v[70:73]
	v_mfma_f32_16x16x32_f16 v[34:37], v[224:227], v[228:231], v[34:37]
	ds_read_b128 v[180:183], v100 offset:256
	ds_read_b128 v[220:223], v100 offset:16640
	ds_read_b128 v[224:227], v100 offset:33024
	ds_read_b128 v[228:231], v100 offset:49408
	s_add_i32 s8, s22, 0xfffb8000
	s_waitcnt vmcnt(15) lgkmcnt(7)
	v_mfma_f32_16x16x32_f16 v[164:167], v[126:129], v[204:207], v[164:167]
	s_waitcnt lgkmcnt(6)
	v_mfma_f32_16x16x32_f16 v[168:171], v[126:129], v[208:211], v[168:171]
	s_waitcnt lgkmcnt(5)
	v_mfma_f32_16x16x32_f16 v[172:175], v[126:129], v[212:215], v[172:175]
	s_waitcnt lgkmcnt(4)
	v_mfma_f32_16x16x32_f16 v[82:85], v[126:129], v[216:219], v[82:85]
	s_waitcnt vmcnt(14)
	v_mfma_f32_16x16x32_f16 v[58:61], v[136:139], v[204:207], v[58:61]
	v_mfma_f32_16x16x32_f16 v[86:89], v[136:139], v[208:211], v[86:89]
	v_mfma_f32_16x16x32_f16 v[94:97], v[136:139], v[212:215], v[94:97]
	v_mfma_f32_16x16x32_f16 v[70:73], v[136:139], v[216:219], v[70:73]
	s_waitcnt vmcnt(13)
	v_mfma_f32_16x16x32_f16 v[54:57], v[184:187], v[204:207], v[54:57]
	v_mfma_f32_16x16x32_f16 v[74:77], v[184:187], v[208:211], v[74:77]
	v_mfma_f32_16x16x32_f16 v[90:93], v[184:187], v[212:215], v[90:93]
	v_mfma_f32_16x16x32_f16 v[62:65], v[184:187], v[216:219], v[62:65]
	s_waitcnt vmcnt(12)
	v_mfma_f32_16x16x32_f16 v[38:41], v[188:191], v[204:207], v[38:41]
	buffer_load_dwordx4 v[126:129], v147, s[16:19], s8 offen
	buffer_load_dwordx4 v[136:139], v148, s[16:19], s8 offen
	buffer_load_dwordx4 v[184:187], v149, s[16:19], s8 offen
	buffer_load_dwordx4 v[204:207], v150, s[16:19], s8 offen
	v_mfma_f32_16x16x32_f16 v[42:45], v[188:191], v[208:211], v[42:45]
	v_mfma_f32_16x16x32_f16 v[46:49], v[188:191], v[212:215], v[46:49]
	v_mfma_f32_16x16x32_f16 v[34:37], v[188:191], v[216:219], v[34:37]
	ds_read_b128 v[188:191], v111 offset:512
	ds_read_b128 v[208:211], v111 offset:16896
	ds_read_b128 v[212:215], v111 offset:33280
	ds_read_b128 v[216:219], v111 offset:49664
	s_add_i32 s8, s22, 0xfffc0000
	s_waitcnt vmcnt(15) lgkmcnt(7)
	v_mfma_f32_16x16x32_f16 v[164:167], v[78:81], v[180:183], v[164:167]
	s_waitcnt lgkmcnt(6)
	v_mfma_f32_16x16x32_f16 v[168:171], v[78:81], v[220:223], v[168:171]
	s_waitcnt lgkmcnt(5)
	v_mfma_f32_16x16x32_f16 v[172:175], v[78:81], v[224:227], v[172:175]
	s_waitcnt lgkmcnt(4)
	v_mfma_f32_16x16x32_f16 v[78:81], v[78:81], v[228:231], v[82:85]
	s_waitcnt vmcnt(14)
	v_mfma_f32_16x16x32_f16 v[58:61], v[122:125], v[180:183], v[58:61]
	v_mfma_f32_16x16x32_f16 v[82:85], v[122:125], v[220:223], v[86:89]
	v_mfma_f32_16x16x32_f16 v[86:89], v[122:125], v[224:227], v[94:97]
	v_mfma_f32_16x16x32_f16 v[70:73], v[122:125], v[228:231], v[70:73]
	s_waitcnt vmcnt(13)
	v_mfma_f32_16x16x32_f16 v[54:57], v[156:159], v[180:183], v[54:57]
	v_mfma_f32_16x16x32_f16 v[74:77], v[156:159], v[220:223], v[74:77]
	v_mfma_f32_16x16x32_f16 v[90:93], v[156:159], v[224:227], v[90:93]
	v_mfma_f32_16x16x32_f16 v[62:65], v[156:159], v[228:231], v[62:65]
	s_waitcnt vmcnt(12)
	v_mfma_f32_16x16x32_f16 v[38:41], v[160:163], v[180:183], v[38:41]
	buffer_load_dwordx4 v[94:97], v147, s[16:19], s8 offen
	buffer_load_dwordx4 v[122:125], v148, s[16:19], s8 offen
	buffer_load_dwordx4 v[156:159], v149, s[16:19], s8 offen
	buffer_load_dwordx4 v[180:183], v150, s[16:19], s8 offen
	v_mfma_f32_16x16x32_f16 v[42:45], v[160:163], v[220:223], v[42:45]
	v_mfma_f32_16x16x32_f16 v[46:49], v[160:163], v[224:227], v[46:49]
	v_mfma_f32_16x16x32_f16 v[34:37], v[160:163], v[228:231], v[34:37]
	ds_read_b128 v[160:163], v98 offset:512
	ds_read_b128 v[220:223], v98 offset:16896
	ds_read_b128 v[224:227], v98 offset:33280
	ds_read_b128 v[228:231], v98 offset:49664
	s_add_i32 s8, s22, 0xfffc8000
	s_waitcnt vmcnt(15) lgkmcnt(7)
	v_mfma_f32_16x16x32_f16 v[164:167], v[66:69], v[188:191], v[164:167]
	s_waitcnt lgkmcnt(6)
	v_mfma_f32_16x16x32_f16 v[168:171], v[66:69], v[208:211], v[168:171]
	s_waitcnt lgkmcnt(5)
	v_mfma_f32_16x16x32_f16 v[172:175], v[66:69], v[212:215], v[172:175]
	s_waitcnt lgkmcnt(4)
	v_mfma_f32_16x16x32_f16 v[66:69], v[66:69], v[216:219], v[78:81]
	s_waitcnt vmcnt(14)
	v_mfma_f32_16x16x32_f16 v[58:61], v[192:195], v[188:191], v[58:61]
	v_mfma_f32_16x16x32_f16 v[78:81], v[192:195], v[208:211], v[82:85]
	v_mfma_f32_16x16x32_f16 v[82:85], v[192:195], v[212:215], v[86:89]
	v_mfma_f32_16x16x32_f16 v[70:73], v[192:195], v[216:219], v[70:73]
	s_waitcnt vmcnt(13)
	v_mfma_f32_16x16x32_f16 v[54:57], v[196:199], v[188:191], v[54:57]
	v_mfma_f32_16x16x32_f16 v[74:77], v[196:199], v[208:211], v[74:77]
	v_mfma_f32_16x16x32_f16 v[86:89], v[196:199], v[212:215], v[90:93]
	v_mfma_f32_16x16x32_f16 v[62:65], v[196:199], v[216:219], v[62:65]
	s_waitcnt vmcnt(12)
	v_mfma_f32_16x16x32_f16 v[38:41], v[200:203], v[188:191], v[38:41]
	buffer_load_dwordx4 v[90:93], v147, s[16:19], s8 offen
	buffer_load_dwordx4 v[188:191], v148, s[16:19], s8 offen
	buffer_load_dwordx4 v[192:195], v149, s[16:19], s8 offen
	buffer_load_dwordx4 v[196:199], v150, s[16:19], s8 offen
	v_mfma_f32_16x16x32_f16 v[42:45], v[200:203], v[208:211], v[42:45]
	v_mfma_f32_16x16x32_f16 v[46:49], v[200:203], v[212:215], v[46:49]
	v_mfma_f32_16x16x32_f16 v[34:37], v[200:203], v[216:219], v[34:37]
	ds_read_b128 v[200:203], v99 offset:512
	ds_read_b128 v[208:211], v99 offset:16896
	ds_read_b128 v[212:215], v99 offset:33280
	ds_read_b128 v[216:219], v99 offset:49664
	s_add_i32 s8, s22, 0xfffd0000
	s_waitcnt vmcnt(15) lgkmcnt(7)
	v_mfma_f32_16x16x32_f16 v[164:167], v[50:53], v[160:163], v[164:167]
	s_waitcnt lgkmcnt(6)
	v_mfma_f32_16x16x32_f16 v[168:171], v[50:53], v[220:223], v[168:171]
	s_waitcnt lgkmcnt(5)
	v_mfma_f32_16x16x32_f16 v[172:175], v[50:53], v[224:227], v[172:175]
	s_waitcnt lgkmcnt(4)
	v_mfma_f32_16x16x32_f16 v[50:53], v[50:53], v[228:231], v[66:69]
	s_waitcnt vmcnt(14)
	v_mfma_f32_16x16x32_f16 v[58:61], v[140:143], v[160:163], v[58:61]
	v_mfma_f32_16x16x32_f16 v[66:69], v[140:143], v[220:223], v[78:81]
	v_mfma_f32_16x16x32_f16 v[78:81], v[140:143], v[224:227], v[82:85]
	v_mfma_f32_16x16x32_f16 v[70:73], v[140:143], v[228:231], v[70:73]
	s_waitcnt vmcnt(13)
	v_mfma_f32_16x16x32_f16 v[54:57], v[152:155], v[160:163], v[54:57]
	v_mfma_f32_16x16x32_f16 v[74:77], v[152:155], v[220:223], v[74:77]
	v_mfma_f32_16x16x32_f16 v[82:85], v[152:155], v[224:227], v[86:89]
	v_mfma_f32_16x16x32_f16 v[62:65], v[152:155], v[228:231], v[62:65]
	s_waitcnt vmcnt(12)
	v_mfma_f32_16x16x32_f16 v[38:41], v[176:179], v[160:163], v[38:41]
	buffer_load_dwordx4 v[86:89], v147, s[16:19], s8 offen
	buffer_load_dwordx4 v[140:143], v148, s[16:19], s8 offen
	buffer_load_dwordx4 v[152:155], v149, s[16:19], s8 offen
	buffer_load_dwordx4 v[160:163], v150, s[16:19], s8 offen
	v_mfma_f32_16x16x32_f16 v[42:45], v[176:179], v[220:223], v[42:45]
	v_mfma_f32_16x16x32_f16 v[46:49], v[176:179], v[224:227], v[46:49]
	v_mfma_f32_16x16x32_f16 v[34:37], v[176:179], v[228:231], v[34:37]
	ds_read_b128 v[176:179], v100 offset:512
	ds_read_b128 v[220:223], v100 offset:16896
	ds_read_b128 v[224:227], v100 offset:33280
	ds_read_b128 v[228:231], v100 offset:49664
	s_add_i32 s8, s22, 0xfffd8000
	s_waitcnt vmcnt(15) lgkmcnt(7)
	v_mfma_f32_16x16x32_f16 v[164:167], v[126:129], v[200:203], v[164:167]
	s_waitcnt lgkmcnt(6)
	v_mfma_f32_16x16x32_f16 v[168:171], v[126:129], v[208:211], v[168:171]
	s_waitcnt lgkmcnt(5)
	v_mfma_f32_16x16x32_f16 v[172:175], v[126:129], v[212:215], v[172:175]
	s_waitcnt lgkmcnt(4)
	v_mfma_f32_16x16x32_f16 v[50:53], v[126:129], v[216:219], v[50:53]
	s_waitcnt vmcnt(14)
	v_mfma_f32_16x16x32_f16 v[58:61], v[136:139], v[200:203], v[58:61]
	v_mfma_f32_16x16x32_f16 v[66:69], v[136:139], v[208:211], v[66:69]
	v_mfma_f32_16x16x32_f16 v[78:81], v[136:139], v[212:215], v[78:81]
	v_mfma_f32_16x16x32_f16 v[70:73], v[136:139], v[216:219], v[70:73]
	s_waitcnt vmcnt(13)
	v_mfma_f32_16x16x32_f16 v[54:57], v[184:187], v[200:203], v[54:57]
	v_mfma_f32_16x16x32_f16 v[74:77], v[184:187], v[208:211], v[74:77]
	v_mfma_f32_16x16x32_f16 v[82:85], v[184:187], v[212:215], v[82:85]
	v_mfma_f32_16x16x32_f16 v[62:65], v[184:187], v[216:219], v[62:65]
	s_waitcnt vmcnt(12)
	v_mfma_f32_16x16x32_f16 v[38:41], v[204:207], v[200:203], v[38:41]
	buffer_load_dwordx4 v[126:129], v147, s[16:19], s8 offen
	buffer_load_dwordx4 v[136:139], v148, s[16:19], s8 offen
	buffer_load_dwordx4 v[184:187], v149, s[16:19], s8 offen
	buffer_load_dwordx4 v[200:203], v150, s[16:19], s8 offen
	v_mfma_f32_16x16x32_f16 v[42:45], v[204:207], v[208:211], v[42:45]
	v_mfma_f32_16x16x32_f16 v[46:49], v[204:207], v[212:215], v[46:49]
	v_mfma_f32_16x16x32_f16 v[34:37], v[204:207], v[216:219], v[34:37]
	ds_read_b128 v[204:207], v111 offset:768
	ds_read_b128 v[208:211], v111 offset:17152
	ds_read_b128 v[212:215], v111 offset:33536
	ds_read_b128 v[216:219], v111 offset:49920
	s_add_i32 s8, s22, 0xfffe0000
	s_waitcnt vmcnt(15) lgkmcnt(7)
	v_mfma_f32_16x16x32_f16 v[164:167], v[94:97], v[176:179], v[164:167]
	s_waitcnt lgkmcnt(6)
	v_mfma_f32_16x16x32_f16 v[168:171], v[94:97], v[220:223], v[168:171]
	s_waitcnt vmcnt(14)
	v_mfma_f32_16x16x32_f16 v[58:61], v[122:125], v[176:179], v[58:61]
	v_mfma_f32_16x16x32_f16 v[66:69], v[122:125], v[220:223], v[66:69]
	s_waitcnt lgkmcnt(5)
	v_mfma_f32_16x16x32_f16 v[78:81], v[122:125], v[224:227], v[78:81]
	s_waitcnt lgkmcnt(4)
	v_mfma_f32_16x16x32_f16 v[70:73], v[122:125], v[228:231], v[70:73]
	s_waitcnt vmcnt(13)
	v_mfma_f32_16x16x32_f16 v[54:57], v[156:159], v[176:179], v[54:57]
	v_mfma_f32_16x16x32_f16 v[74:77], v[156:159], v[220:223], v[74:77]
	v_mfma_f32_16x16x32_f16 v[82:85], v[156:159], v[224:227], v[82:85]
	v_mfma_f32_16x16x32_f16 v[62:65], v[156:159], v[228:231], v[62:65]
	s_waitcnt vmcnt(12)
	v_mfma_f32_16x16x32_f16 v[38:41], v[180:183], v[176:179], v[38:41]
	v_mfma_f32_16x16x32_f16 v[42:45], v[180:183], v[220:223], v[42:45]
	buffer_load_dwordx4 v[122:125], v147, s[16:19], s8 offen
	buffer_load_dwordx4 v[156:159], v148, s[16:19], s8 offen
	buffer_load_dwordx4 v[176:179], v149, s[16:19], s8 offen
	buffer_load_dwordx4 v[220:223], v150, s[16:19], s8 offen
	v_mfma_f32_16x16x32_f16 v[50:53], v[94:97], v[228:231], v[50:53]
	v_mfma_f32_16x16x32_f16 v[46:49], v[180:183], v[224:227], v[46:49]
	v_mfma_f32_16x16x32_f16 v[34:37], v[180:183], v[228:231], v[34:37]
	v_mfma_f32_16x16x32_f16 v[172:175], v[94:97], v[224:227], v[172:175]
	ds_read_b128 v[94:97], v98 offset:768
	ds_read_b128 v[180:183], v98 offset:17152
	ds_read_b128 v[224:227], v98 offset:33536
	ds_read_b128 v[228:231], v98 offset:49920
	s_add_i32 s8, s22, 0xfffe8000
	s_waitcnt vmcnt(15) lgkmcnt(7)
	v_mfma_f32_16x16x32_f16 v[164:167], v[90:93], v[204:207], v[164:167]
	s_waitcnt lgkmcnt(6)
	v_mfma_f32_16x16x32_f16 v[168:171], v[90:93], v[208:211], v[168:171]
	s_waitcnt lgkmcnt(5)
	v_mfma_f32_16x16x32_f16 v[172:175], v[90:93], v[212:215], v[172:175]
	s_waitcnt lgkmcnt(4)
	v_mfma_f32_16x16x32_f16 v[90:93], v[90:93], v[216:219], v[50:53]
	s_waitcnt vmcnt(14)
	v_mfma_f32_16x16x32_f16 v[232:235], v[188:191], v[204:207], v[58:61]
	v_mfma_f32_16x16x32_f16 v[66:69], v[188:191], v[208:211], v[66:69]
	v_mfma_f32_16x16x32_f16 v[78:81], v[188:191], v[212:215], v[78:81]
	v_mfma_f32_16x16x32_f16 v[70:73], v[188:191], v[216:219], v[70:73]
	s_waitcnt vmcnt(13)
	v_mfma_f32_16x16x32_f16 v[188:191], v[192:195], v[204:207], v[54:57]
	v_mfma_f32_16x16x32_f16 v[74:77], v[192:195], v[208:211], v[74:77]
	v_mfma_f32_16x16x32_f16 v[82:85], v[192:195], v[212:215], v[82:85]
	v_mfma_f32_16x16x32_f16 v[62:65], v[192:195], v[216:219], v[62:65]
	s_waitcnt vmcnt(12)
	v_mfma_f32_16x16x32_f16 v[192:195], v[196:199], v[204:207], v[38:41]
	buffer_load_dwordx4 v[58:61], v147, s[16:19], s8 offen
	buffer_load_dwordx4 v[54:57], v148, s[16:19], s8 offen
	buffer_load_dwordx4 v[50:53], v149, s[16:19], s8 offen
	buffer_load_dwordx4 v[38:41], v150, s[16:19], s8 offen
	v_mfma_f32_16x16x32_f16 v[42:45], v[196:199], v[208:211], v[42:45]
	v_mfma_f32_16x16x32_f16 v[46:49], v[196:199], v[212:215], v[46:49]
	v_mfma_f32_16x16x32_f16 v[196:199], v[196:199], v[216:219], v[34:37]
	ds_read_b128 v[204:207], v99 offset:768
	ds_read_b128 v[208:211], v99 offset:17152
	ds_read_b128 v[212:215], v99 offset:33536
	ds_read_b128 v[216:219], v99 offset:49920
	s_add_i32 s8, s22, 0xffff0000
	s_waitcnt vmcnt(15) lgkmcnt(7)
	v_mfma_f32_16x16x32_f16 v[164:167], v[86:89], v[94:97], v[164:167]
	s_waitcnt lgkmcnt(6)
	v_mfma_f32_16x16x32_f16 v[168:171], v[86:89], v[180:183], v[168:171]
	s_waitcnt lgkmcnt(5)
	v_mfma_f32_16x16x32_f16 v[172:175], v[86:89], v[224:227], v[172:175]
	s_waitcnt lgkmcnt(4)
	v_mfma_f32_16x16x32_f16 v[86:89], v[86:89], v[228:231], v[90:93]
	s_waitcnt vmcnt(14)
	v_mfma_f32_16x16x32_f16 v[232:235], v[140:143], v[94:97], v[232:235]
	v_mfma_f32_16x16x32_f16 v[66:69], v[140:143], v[180:183], v[66:69]
	v_mfma_f32_16x16x32_f16 v[236:239], v[140:143], v[224:227], v[78:81]
	v_mfma_f32_16x16x32_f16 v[70:73], v[140:143], v[228:231], v[70:73]
	s_waitcnt vmcnt(13)
	v_mfma_f32_16x16x32_f16 v[140:143], v[152:155], v[94:97], v[188:191]
	v_mfma_f32_16x16x32_f16 v[74:77], v[152:155], v[180:183], v[74:77]
	v_mfma_f32_16x16x32_f16 v[82:85], v[152:155], v[224:227], v[82:85]
	v_mfma_f32_16x16x32_f16 v[62:65], v[152:155], v[228:231], v[62:65]
	s_waitcnt vmcnt(12)
	v_mfma_f32_16x16x32_f16 v[152:155], v[160:163], v[94:97], v[192:195]
	buffer_load_dwordx4 v[94:97], v147, s[16:19], s8 offen
	buffer_load_dwordx4 v[90:93], v148, s[16:19], s8 offen
	buffer_load_dwordx4 v[78:81], v149, s[16:19], s8 offen
	buffer_load_dwordx4 v[34:37], v150, s[16:19], s8 offen
	v_mfma_f32_16x16x32_f16 v[42:45], v[160:163], v[180:183], v[42:45]
	v_mfma_f32_16x16x32_f16 v[46:49], v[160:163], v[224:227], v[46:49]
	v_mfma_f32_16x16x32_f16 v[160:163], v[160:163], v[228:231], v[196:199]
	ds_read_b128 v[180:183], v100 offset:768
	ds_read_b128 v[188:191], v100 offset:17152
	ds_read_b128 v[192:195], v100 offset:33536
	ds_read_b128 v[196:199], v100 offset:49920
	s_add_i32 s8, s22, 0xffff8000
	s_waitcnt vmcnt(15) lgkmcnt(7)
	v_mfma_f32_16x16x32_f16 v[164:167], v[126:129], v[204:207], v[164:167]
	s_waitcnt lgkmcnt(6)
	v_mfma_f32_16x16x32_f16 v[168:171], v[126:129], v[208:211], v[168:171]
	s_waitcnt lgkmcnt(5)
	v_mfma_f32_16x16x32_f16 v[172:175], v[126:129], v[212:215], v[172:175]
	s_waitcnt lgkmcnt(4)
	v_mfma_f32_16x16x32_f16 v[86:89], v[126:129], v[216:219], v[86:89]
	s_waitcnt vmcnt(14)
	v_mfma_f32_16x16x32_f16 v[126:129], v[136:139], v[204:207], v[232:235]
	v_mfma_f32_16x16x32_f16 v[66:69], v[136:139], v[208:211], v[66:69]
	v_mfma_f32_16x16x32_f16 v[224:227], v[136:139], v[212:215], v[236:239]
	v_mfma_f32_16x16x32_f16 v[136:139], v[136:139], v[216:219], v[70:73]
	s_waitcnt vmcnt(13)
	v_mfma_f32_16x16x32_f16 v[140:143], v[184:187], v[204:207], v[140:143]
	v_mfma_f32_16x16x32_f16 v[74:77], v[184:187], v[208:211], v[74:77]
	v_mfma_f32_16x16x32_f16 v[228:231], v[184:187], v[212:215], v[82:85]
	v_mfma_f32_16x16x32_f16 v[184:187], v[184:187], v[216:219], v[62:65]
	s_waitcnt vmcnt(12)
	v_mfma_f32_16x16x32_f16 v[152:155], v[200:203], v[204:207], v[152:155]
	v_mfma_f32_16x16x32_f16 v[204:207], v[200:203], v[208:211], v[42:45]
	buffer_load_dwordx4 v[82:85], v147, s[16:19], s8 offen
	buffer_load_dwordx4 v[70:73], v148, s[16:19], s8 offen
	buffer_load_dwordx4 v[62:65], v149, s[16:19], s8 offen
	buffer_load_dwordx4 v[42:45], v150, s[16:19], s8 offen
	v_mfma_f32_16x16x32_f16 v[46:49], v[200:203], v[212:215], v[46:49]
	v_mfma_f32_16x16x32_f16 v[160:163], v[200:203], v[216:219], v[160:163]
	v_add_u32_e32 v0, 0x1ac00, v104
	ds_read_b128 v[240:243], v0
	ds_read_b128 v[244:247], v0 offset:16
	s_waitcnt vmcnt(12) lgkmcnt(5)
	v_mfma_f32_16x16x32_f16 v[164:167], v[122:125], v[180:183], v[164:167]
	v_mfma_f32_16x16x32_f16 v[126:129], v[156:159], v[180:183], v[126:129]
	v_mfma_f32_16x16x32_f16 v[140:143], v[176:179], v[180:183], v[140:143]
	v_mfma_f32_16x16x32_f16 v[152:155], v[220:223], v[180:183], v[152:155]
	s_waitcnt lgkmcnt(4)
	v_mfma_f32_16x16x32_f16 v[168:171], v[122:125], v[188:191], v[168:171]
	v_mfma_f32_16x16x32_f16 v[208:211], v[156:159], v[188:191], v[66:69]
	v_mfma_f32_16x16x32_f16 v[212:215], v[176:179], v[188:191], v[74:77]
	v_mfma_f32_16x16x32_f16 v[204:207], v[220:223], v[188:191], v[204:207]
	s_waitcnt lgkmcnt(3)
	v_mfma_f32_16x16x32_f16 v[172:175], v[122:125], v[192:195], v[172:175]
	v_cvt_pk_f16_f32 v232, v164, v165
	v_cvt_pk_f16_f32 v233, v166, v167
	v_pk_max_f16 v232, v232, 0
	v_pk_max_f16 v233, v233, 0
	v_mfma_f32_16x16x32_f16 v[224:227], v[156:159], v[192:195], v[224:227]
	v_cvt_pk_f16_f32 v234, v126, v127
	v_cvt_pk_f16_f32 v235, v128, v129
	v_pk_max_f16 v234, v234, 0
	v_pk_max_f16 v235, v235, 0
	v_mfma_f32_16x16x32_f16 v[228:231], v[176:179], v[192:195], v[228:231]
	v_cvt_pk_f16_f32 v236, v140, v141
	v_cvt_pk_f16_f32 v237, v142, v143
	v_pk_max_f16 v236, v236, 0
	v_pk_max_f16 v237, v237, 0
	v_mfma_f32_16x16x32_f16 v[216:219], v[220:223], v[192:195], v[46:49]
	v_cvt_pk_f16_f32 v238, v152, v153
	v_cvt_pk_f16_f32 v239, v154, v155
	v_pk_max_f16 v238, v238, 0
	v_pk_max_f16 v239, v239, 0
	s_waitcnt lgkmcnt(2)
	v_mfma_f32_16x16x32_f16 v[200:203], v[122:125], v[196:199], v[86:89]
	v_cvt_pk_f16_f32 v180, v168, v169
	v_cvt_pk_f16_f32 v181, v170, v171
	v_pk_max_f16 v180, v180, 0
	v_pk_max_f16 v181, v181, 0
	buffer_load_dwordx4 v[86:89], v147, s[16:19], s22 offen
	buffer_load_dwordx4 v[74:77], v148, s[16:19], s22 offen
	buffer_load_dwordx4 v[66:69], v149, s[16:19], s22 offen
	buffer_load_dwordx4 v[46:49], v150, s[16:19], s22 offen
	v_mfma_f32_16x16x32_f16 v[136:139], v[156:159], v[196:199], v[136:139]
	v_cvt_pk_f16_f32 v182, v208, v209
	v_cvt_pk_f16_f32 v183, v210, v211
	v_pk_max_f16 v182, v182, 0
	v_pk_max_f16 v183, v183, 0
	s_waitcnt lgkmcnt(1)
	v_mfma_f32_16x16x32_f16 v[252:255], v[240:243], v[232:235], 0
	v_mfma_f32_16x16x32_f16 v[184:187], v[176:179], v[196:199], v[184:187]
	v_cvt_pk_f16_f32 v188, v212, v213
	v_cvt_pk_f16_f32 v189, v214, v215
	v_pk_max_f16 v188, v188, 0
	v_pk_max_f16 v189, v189, 0
	s_waitcnt lgkmcnt(0)
	v_mfma_f32_16x16x32_f16 v[252:255], v[244:247], v[236:239], v[252:255]
	v_mfma_f32_16x16x32_f16 v[160:163], v[220:223], v[196:199], v[160:163]
	v_cvt_pk_f16_f32 v190, v204, v205
	v_cvt_pk_f16_f32 v191, v206, v207
	v_pk_max_f16 v190, v190, 0
	v_pk_max_f16 v191, v191, 0
	v_cvt_pk_f16_f32 v232, v172, v173
	v_cvt_pk_f16_f32 v233, v174, v175
	v_pk_max_f16 v232, v232, 0
	v_pk_max_f16 v233, v233, 0
	v_cvt_pk_f16_f32 v234, v224, v225
	v_cvt_pk_f16_f32 v235, v226, v227
	v_pk_max_f16 v234, v234, 0
	v_pk_max_f16 v235, v235, 0
	v_mfma_f32_16x16x32_f16 v[192:195], v[240:243], v[180:183], 0
	v_cvt_pk_f16_f32 v236, v228, v229
	v_cvt_pk_f16_f32 v237, v230, v231
	v_pk_max_f16 v236, v236, 0
	v_pk_max_f16 v237, v237, 0
	v_mfma_f32_16x16x32_f16 v[192:195], v[244:247], v[188:191], v[192:195]
	v_cvt_pk_f16_f32 v238, v216, v217
	v_cvt_pk_f16_f32 v239, v218, v219
	v_pk_max_f16 v238, v238, 0
	v_pk_max_f16 v239, v239, 0
	v_cvt_pk_f16_f32 v180, v200, v201
	v_cvt_pk_f16_f32 v181, v202, v203
	v_pk_max_f16 v180, v180, 0
	v_pk_max_f16 v181, v181, 0
	v_mfma_f32_16x16x32_f16 v[196:199], v[240:243], v[232:235], 0
	v_cvt_pk_f16_f32 v182, v136, v137
	v_cvt_pk_f16_f32 v183, v138, v139
	v_pk_max_f16 v182, v182, 0
	v_pk_max_f16 v183, v183, 0
	v_mfma_f32_16x16x32_f16 v[196:199], v[244:247], v[236:239], v[196:199]
	v_cvt_pk_f16_f32 v188, v184, v185
	v_cvt_pk_f16_f32 v189, v186, v187
	v_pk_max_f16 v188, v188, 0
	v_pk_max_f16 v189, v189, 0
	v_cvt_pk_f16_f32 v190, v160, v161
	v_cvt_pk_f16_f32 v191, v162, v163
	v_pk_max_f16 v190, v190, 0
	v_pk_max_f16 v191, v191, 0
	v_mfma_f32_16x16x32_f16 v[122:125], v[240:243], v[180:183], 0
	s_nop 0
	v_mfma_f32_16x16x32_f16 v[122:125], v[244:247], v[188:191], v[122:125]
	s_load_dword s30, s[12:13], 0x0
	v_cndmask_b32_e64 v0, v252, v192, s[2:3]
	v_cndmask_b32_e64 v0, v0, v196, s[0:1]
	s_nop 4
	v_cndmask_b32_e64 v0, v0, v122, s[26:27]
	ds_write_b32 v112, v0
	s_waitcnt lgkmcnt(0)
	s_barrier
	ds_read_b128 v[232:235], v113
	ds_read_b128 v[236:239], v113 offset:1024
	ds_read_u16 v248, v114
	ds_read_u16 v249, v114 offset:512
	ds_read_u16 v250, v114 offset:1024
	ds_read_u16 v251, v114 offset:1536
	s_and_b64 vcc, exec, s[4:5]
	s_waitcnt lgkmcnt(4)
	v_add_f32_e32 v0, v232, v233
	v_add_f32_e32 v1, v234, v235
	v_add_f32_e32 v121, v236, v237
	v_add_f32_e32 v144, v238, v239
	v_add_f32_e32 v0, v0, v1
	v_add_f32_e32 v121, v121, v144
	v_add_f32_e32 v0, v0, v121
	v_add_f32_e32 v0, s30, v0
	s_cbranch_vccnz .Lskip_out
	ds_write_b32 v106, v0
.Lskip_out:
	v_mov_b32_e32 v1, v0
	s_nop 1
	v_permlane16_swap_b32_e32 v0, v1
	v_mov_b32_e32 v121, v0
	v_mov_b32_e32 v144, v1
	s_nop 1
	v_permlane32_swap_b32_e32 v0, v121
	v_permlane32_swap_b32_e32 v1, v144
	s_branch .LBB1_3

	.amdhsa_kernel _Z16pdag_main_kernelPKfS0_S0_PKDv8_DF16_S3_S0_PKDF16_S5_S0_Pf
		.amdhsa_group_segment_fixed_size 130304
		.amdhsa_private_segment_fixed_size 0
		.amdhsa_kernarg_size 80
		.amdhsa_user_sgpr_count 2
		.amdhsa_user_sgpr_dispatch_ptr 0
		.amdhsa_user_sgpr_queue_ptr 0
		.amdhsa_user_sgpr_kernarg_segment_ptr 1
		.amdhsa_user_sgpr_dispatch_id 0
		.amdhsa_user_sgpr_kernarg_preload_length 0
		.amdhsa_user_sgpr_kernarg_preload_offset 0
		.amdhsa_user_sgpr_private_segment_size 0
		.amdhsa_uses_dynamic_stack 0
		.amdhsa_enable_private_segment 0
		.amdhsa_system_sgpr_workgroup_id_x 1
		.amdhsa_system_sgpr_workgroup_id_y 0
		.amdhsa_system_sgpr_workgroup_id_z 0
		.amdhsa_system_sgpr_workgroup_info 0
		.amdhsa_system_vgpr_workitem_id 0
		.amdhsa_next_free_vgpr 256
		.amdhsa_next_free_sgpr 96
		.amdhsa_accum_offset 256
		.amdhsa_reserve_vcc 1
		.amdhsa_float_round_mode_32 0
		.amdhsa_float_round_mode_16_64 0
		.amdhsa_float_denorm_mode_32 3
		.amdhsa_float_denorm_mode_16_64 3
		.amdhsa_dx10_clamp 1
		.amdhsa_ieee_mode 1
		.amdhsa_fp16_overflow 0
		.amdhsa_tg_split 0
		.amdhsa_exception_fp_ieee_invalid_op 0
		.amdhsa_exception_fp_denorm_src 0
		.amdhsa_exception_fp_ieee_div_zero 0
		.amdhsa_exception_fp_ieee_overflow 0
		.amdhsa_exception_fp_ieee_underflow 0
		.amdhsa_exception_fp_ieee_inexact 0
		.amdhsa_exception_int_div_zero 0
	.end_amdhsa_kernel

amdhsa.kernels:
  - .agpr_count:     0
    .args:
      - .actual_access:  read_only
        .address_space:  global
        .offset:         0
        .size:           8
        .value_kind:     global_buffer
      - .actual_access:  write_only
        .address_space:  global
        .offset:         8
        .size:           8
        .value_kind:     global_buffer
      - .actual_access:  read_only
        .address_space:  global
        .offset:         16
        .size:           8
        .value_kind:     global_buffer
      - .actual_access:  read_only
        .address_space:  global
        .offset:         24
        .size:           8
        .value_kind:     global_buffer
      - .actual_access:  read_only
        .address_space:  global
        .offset:         32
        .size:           8
        .value_kind:     global_buffer
      - .actual_access:  read_only
        .address_space:  global
        .offset:         40
        .size:           8
        .value_kind:     global_buffer
      - .actual_access:  read_only
        .address_space:  global
        .offset:         48
        .size:           8
        .value_kind:     global_buffer
      - .actual_access:  read_only
        .address_space:  global
        .offset:         56
        .size:           8
        .value_kind:     global_buffer
      - .actual_access:  read_only
        .address_space:  global
        .offset:         64
        .size:           8
        .value_kind:     global_buffer
      - .actual_access:  read_only
        .address_space:  global
        .offset:         72
        .size:           8
        .value_kind:     global_buffer
      - .actual_access:  read_only
        .address_space:  global
        .offset:         80
        .size:           8
        .value_kind:     global_buffer
      - .actual_access:  write_only
        .address_space:  global
        .offset:         88
        .size:           8
        .value_kind:     global_buffer
      - .actual_access:  write_only
        .address_space:  global
        .offset:         96
        .size:           8
        .value_kind:     global_buffer
      - .actual_access:  write_only
        .address_space:  global
        .offset:         104
        .size:           8
        .value_kind:     global_buffer
      - .actual_access:  write_only
        .address_space:  global
        .offset:         112
        .size:           8
        .value_kind:     global_buffer
      - .actual_access:  write_only
        .address_space:  global
        .offset:         120
        .size:           8
        .value_kind:     global_buffer
    .group_segment_fixed_size: 17440
    .kernarg_segment_align: 8
    .kernarg_segment_size: 128
    .language:       OpenCL C
    .language_version:
      - 2
      - 0
    .max_flat_workgroup_size: 256
    .name:           _Z11prep_kernelPKfPDv8_DF16_S0_S0_S0_S0_S0_S0_S0_S0_S0_S2_PfPDF16_S4_S3_
    .private_segment_fixed_size: 0
    .sgpr_count:     32
    .sgpr_spill_count: 0
    .symbol:         _Z11prep_kernelPKfPDv8_DF16_S0_S0_S0_S0_S0_S0_S0_S0_S0_S2_PfPDF16_S4_S3_.kd
    .uniform_work_group_size: 1
    .uses_dynamic_stack: false
    .vgpr_count:     42
    .vgpr_spill_count: 0
    .wavefront_size: 64
  - .agpr_count:     0
    .args:
      - .actual_access:  read_only
        .address_space:  global
        .offset:         0
        .size:           8
        .value_kind:     global_buffer
      - .actual_access:  read_only
        .address_space:  global
        .offset:         8
        .size:           8
        .value_kind:     global_buffer
      - .actual_access:  read_only
        .address_space:  global
        .offset:         16
        .size:           8
        .value_kind:     global_buffer
      - .actual_access:  read_only
        .address_space:  global
        .offset:         24
        .size:           8
        .value_kind:     global_buffer
      - .actual_access:  read_only
        .address_space:  global
        .offset:         32
        .size:           8
        .value_kind:     global_buffer
      - .actual_access:  read_only
        .address_space:  global
        .offset:         40
        .size:           8
        .value_kind:     global_buffer
      - .actual_access:  read_only
        .address_space:  global
        .offset:         48
        .size:           8
        .value_kind:     global_buffer
      - .actual_access:  read_only
        .address_space:  global
        .offset:         56
        .size:           8
        .value_kind:     global_buffer
      - .actual_access:  read_only
        .address_space:  global
        .offset:         64
        .size:           8
        .value_kind:     global_buffer
      - .actual_access:  write_only
        .address_space:  global
        .offset:         72
        .size:           8
        .value_kind:     global_buffer
    .group_segment_fixed_size: 130304
    .kernarg_segment_align: 8
    .kernarg_segment_size: 80
    .language:       OpenCL C
    .language_version:
      - 2
      - 0
    .max_flat_workgroup_size: 512
    .name:           _Z16pdag_main_kernelPKfS0_S0_PKDv8_DF16_S3_S0_PKDF16_S5_S0_Pf
    .private_segment_fixed_size: 0
    .sgpr_count:     40
    .sgpr_spill_count: 0
    .symbol:         _Z16pdag_main_kernelPKfS0_S0_PKDv8_DF16_S3_S0_PKDF16_S5_S0_Pf.kd
    .uniform_work_group_size: 1
    .uses_dynamic_stack: false
    .vgpr_count:     256
    .vgpr_spill_count: 0
    .wavefront_size: 64
